# v7 plus nt on the P1 token-row loads (x, ctx read once here)
# speedup vs baseline: 1.0089x; 1.0089x over previous
.LBB0_114:
	s_lshr_b32 s88, s3, 6
	s_cmp_lt_i32 s28, 2
	s_cselect_b64 s[0:1], -1, 0
	s_cmp_gt_i32 s29, 1
	s_cselect_b64 s[6:7], -1, 0
	s_and_b64 s[0:1], s[0:1], s[6:7]
	s_andn2_b64 vcc, exec, s[0:1]
	s_cbranch_vccnz .LBB0_226
	s_cmpk_gt_i32 s2, 0x47f
	s_cbranch_scc1 .LBB0_172
	s_add_u32 s3, s26, 0x100000
	s_addc_u32 s30, s27, 0
	s_add_u32 s31, s26, 0x35800000
	s_addc_u32 s34, s27, 0
	s_lshl_b32 s0, s88, 9
	s_add_u32 s0, s26, s0
	v_and_b32_e32 v182, 48, v0
	v_mov_b32_e32 v183, 0
	s_addc_u32 s1, s27, 0
	s_waitcnt vmcnt(10)
	v_lshl_add_u64 v[2:3], s[0:1], 0, v[182:183]
	s_mov_b64 s[0:1], 0x600000
	v_lshl_add_u64 v[4:5], v[2:3], 0, s[0:1]
	s_mov_b64 s[0:1], 0x620000
	s_lshl_b32 s8, s88, 10
	s_lshl_b32 s14, s2, 3
	v_lshl_add_u64 v[2:3], v[2:3], 0, s[0:1]
	s_lshl_b32 s1, s88, 13
	s_add_i32 s10, s8, 0
	s_add_i32 s8, s88, s14
	s_add_i32 s1, s1, 0
	s_add_i32 s12, 0, 0x10000
	s_ashr_i32 s9, s8, 31
	s_add_i32 s11, s8, 0xffffe000
	v_lshlrev_b32_e32 v1, 12, v0
	s_cmpk_lt_i32 s8, 0x2000
	v_and_b32_e32 v182, 0xf000, v1
	s_cselect_b32 s9, s9, 0
	s_cselect_b32 s8, s8, s11
	v_or_b32_e32 v6, 0x10000, v182
	v_mov_b32_e32 v7, v183
	v_lshlrev_b32_e32 v184, 2, v230
	v_and_b32_e32 v1, 31, v0
	s_waitcnt lgkmcnt(0)
	s_cselect_b32 s13, s37, s41
	s_cselect_b32 s15, s36, s40
	s_lshl_b64 s[8:9], s[8:9], 13
	s_waitcnt vmcnt(7)
	v_lshl_add_u64 v[54:55], v[4:5], 0, v[182:183]
	s_waitcnt vmcnt(4)
	v_lshl_add_u64 v[62:63], v[4:5], 0, v[6:7]
	v_lshl_add_u64 v[94:95], v[2:3], 0, v[182:183]
	v_lshl_add_u64 v[126:127], v[2:3], 0, v[6:7]
	v_or_b32_e32 v186, 0x400, v184
	v_or_b32_e32 v188, 0x500, v184
	v_or_b32_e32 v190, 0x600, v184
	v_or_b32_e32 v192, 0x700, v184
	v_lshlrev_b32_e32 v182, 2, v1
	s_add_u32 s8, s15, s8
	v_lshl_add_u64 v[194:195], s[70:71], 0, v[182:183]
	v_lshlrev_b32_e32 v182, 4, v230
	v_lshlrev_b32_e32 v168, 2, v186
	v_lshlrev_b32_e32 v170, 2, v188
	v_lshlrev_b32_e32 v172, 2, v190
	v_lshlrev_b32_e32 v174, 2, v192
	global_load_dwordx4 v[2:5], v[54:55], off
	global_load_dwordx4 v[6:9], v[54:55], off offset:64
	global_load_dwordx4 v[10:13], v[62:63], off
	global_load_dwordx4 v[14:17], v[62:63], off offset:64
	global_load_dwordx4 v[18:21], v[54:55], off offset:128
	global_load_dwordx4 v[22:25], v[54:55], off offset:192
	global_load_dwordx4 v[26:29], v[62:63], off offset:128
	global_load_dwordx4 v[30:33], v[62:63], off offset:192
	global_load_dwordx4 v[34:37], v[54:55], off offset:256
	global_load_dwordx4 v[38:41], v[54:55], off offset:320
	global_load_dwordx4 v[42:45], v[62:63], off offset:256
	global_load_dwordx4 v[46:49], v[62:63], off offset:320
	global_load_dwordx4 v[50:53], v[54:55], off offset:384
	s_nop 0
	global_load_dwordx4 v[54:57], v[54:55], off offset:448
	s_addc_u32 s9, s13, s9
	global_load_dwordx4 v[58:61], v[62:63], off offset:384
	s_nop 0
	global_load_dwordx4 v[62:65], v[62:63], off offset:448
	s_nop 0
	global_load_dwordx4 v[66:69], v[94:95], off
	global_load_dwordx4 v[70:73], v[94:95], off offset:64
	global_load_dwordx4 v[74:77], v[94:95], off offset:128
	global_load_dwordx4 v[78:81], v[94:95], off offset:192
	global_load_dwordx4 v[82:85], v[94:95], off offset:256
	global_load_dwordx4 v[86:89], v[94:95], off offset:320
	global_load_dwordx4 v[90:93], v[94:95], off offset:384
	s_nop 0
	global_load_dwordx4 v[94:97], v[94:95], off offset:448
	s_nop 0
	global_load_dwordx4 v[98:101], v[126:127], off
	global_load_dwordx4 v[102:105], v[126:127], off offset:64
	global_load_dwordx4 v[106:109], v[126:127], off offset:128
	global_load_dwordx4 v[110:113], v[126:127], off offset:192
	global_load_dwordx4 v[114:117], v[126:127], off offset:256
	global_load_dwordx4 v[118:121], v[126:127], off offset:320
	global_load_dwordx4 v[122:125], v[126:127], off offset:384
	s_nop 0
	global_load_dwordx4 v[126:129], v[126:127], off offset:448
	s_nop 0
	global_load_dwordx4 v[130:133], v174, s[8:9] nt
	global_load_dwordx4 v[134:137], v172, s[8:9] nt
	global_load_dwordx4 v[138:141], v170, s[8:9] nt
	global_load_dwordx4 v[142:145], v168, s[8:9] nt
	global_load_dwordx4 v[146:149], v182, s[8:9] offset:3072 nt
	global_load_dwordx4 v[150:153], v182, s[8:9] offset:2048 nt
	global_load_dwordx4 v[154:157], v182, s[8:9] offset:1024 nt
	global_load_dwordx4 v[158:161], v182, s[8:9] nt
	v_lshrrev_b32_e32 v163, 4, v230
	v_lshlrev_b32_e32 v187, 5, v163
	v_lshlrev_b32_e32 v163, 7, v163
	v_lshl_add_u32 v163, s88, 8, v163
	v_and_b32_e32 v165, 15, v0
	v_lshlrev_b32_e32 v167, 2, v163
	v_or_b32_e32 v163, v230, v163
	v_cmp_gt_u32_e64 s[6:7], 8, v165
	v_lshl_add_u32 v1, v165, 13, s10
	v_lshlrev_b32_e32 v165, 2, v165
	v_lshlrev_b32_e32 v163, 2, v163
	v_add3_u32 v189, s12, v165, v167
	v_or_b32_e32 v165, 64, v163
	v_add_u32_e32 v191, s12, v165
	v_or_b32_e32 v165, 0xc0, v163
	v_add_u32_e32 v193, s12, v165
	v_or_b32_e32 v165, 0x140, v163
	v_or_b32_e32 v163, 0x1c0, v163
	v_add_u32_e32 v211, s12, v163
	v_mbcnt_lo_u32_b32 v163, -1, 0
	v_mbcnt_hi_u32_b32 v163, -1, v163
	v_add_u32_e32 v210, s12, v165
	v_and_b32_e32 v165, 64, v163
	v_add_u32_e32 v165, 64, v165
	v_xor_b32_e32 v167, 1, v163
	v_cmp_lt_i32_e32 vcc, v167, v165
	v_mov_b32_e32 v185, v183
	s_movk_i32 s0, 0x100
	v_cndmask_b32_e32 v167, v163, v167, vcc
	v_lshlrev_b32_e32 v214, 2, v167
	v_xor_b32_e32 v167, 2, v163
	v_cmp_lt_i32_e32 vcc, v167, v165
	v_lshlrev_b32_e32 v176, 2, v0
	v_mov_b32_e32 v177, v183
	v_cndmask_b32_e32 v167, v163, v167, vcc
	v_lshlrev_b32_e32 v215, 2, v167
	v_xor_b32_e32 v167, 4, v163
	v_cmp_lt_i32_e32 vcc, v167, v165
	v_mov_b32_e32 v169, v183
	v_or_b32_e32 v162, 0x100, v184
	v_cndmask_b32_e32 v167, v163, v167, vcc
	v_lshlrev_b32_e32 v216, 2, v167
	v_xor_b32_e32 v167, 8, v163
	v_cmp_lt_i32_e32 vcc, v167, v165
	v_or_b32_e32 v164, 0x200, v184
	v_or_b32_e32 v166, 0x300, v184
	v_cndmask_b32_e32 v167, v163, v167, vcc
	v_lshlrev_b32_e32 v217, 2, v167
	v_xor_b32_e32 v167, 16, v163
	v_cmp_lt_i32_e32 vcc, v167, v165
	v_cmp_gt_u32_e64 s[10:11], s0, v0
	v_add_u32_e32 v212, s12, v176
	v_cndmask_b32_e32 v167, v163, v167, vcc
	v_lshlrev_b32_e32 v218, 2, v167
	v_xor_b32_e32 v167, 32, v163
	v_cmp_lt_i32_e32 vcc, v167, v165
	v_lshl_add_u64 v[176:177], s[26:27], 0, v[176:177]
	s_mov_b64 s[12:13], 0x200000
	v_add_u32_e32 v213, s1, v182
	v_lshl_add_u64 v[200:201], s[48:49], 0, v[168:169]
	v_mov_b32_e32 v171, v183
	v_mov_b32_e32 v173, v183
	v_mov_b32_e32 v175, v183
	v_cndmask_b32_e32 v163, v163, v167, vcc
	v_lshl_add_u64 v[168:169], s[26:27], 0, v[184:185]
	s_mov_b64 s[0:1], 0xbb600000
	s_lshl_b32 s35, s33, 3
	v_cmp_gt_u32_e64 s[8:9], 32, v230
	v_lshl_add_u64 v[196:197], v[176:177], 0, s[12:13]
	v_lshl_add_u64 v[198:199], s[48:49], 0, v[182:183]
	v_lshl_add_u64 v[202:203], s[48:49], 0, v[170:171]
	v_lshl_add_u64 v[204:205], s[48:49], 0, v[172:173]
	v_lshl_add_u64 v[206:207], s[48:49], 0, v[174:175]
	v_lshlrev_b32_e32 v219, 2, v163
	v_lshl_add_u64 v[208:209], v[168:169], 0, s[0:1]
	s_add_i32 s46, s88, s35
	v_mov_b32_e32 v185, 0x358637bd
	s_mov_b32 s47, 0xf800000
	v_mov_b32_e32 v220, 0x260
	s_mov_b32 s48, 0xc3e00000
	v_lshlrev_b32_e32 v221, 2, v162
	v_lshlrev_b32_e32 v222, 2, v164
	v_lshlrev_b32_e32 v223, 2, v166
	v_mov_b32_e32 v224, 0x43e00000
	s_mov_b32 s49, s2
	s_branch .LBB0_118

.LBB0_150:
	v_mul_f32_e32 v166, 0x41800000, v162
	v_mul_f32_e32 v167, 0x41800000, v163
	v_med3_f32 v166, v166, s48, v224
	v_med3_f32 v167, v167, s48, v224
	v_mov_b32_e32 v175, v183
	v_cvt_pk_fp8_f32 v175, v166, v167
	v_mul_f32_e32 v174, 0x41800000, v164
	v_mul_f32_e32 v166, 0x41800000, v165
	v_med3_f32 v167, v174, s48, v224
	v_med3_f32 v166, v166, s48, v224
	v_cvt_pk_fp8_f32 v175, v167, v166 op_sel:[0,0,1]
	s_add_i32 s49, s49, s33
	s_cmpk_gt_i32 s49, 0x47f
	s_cselect_b64 s[0:1], -1, 0
	s_and_b64 vcc, exec, s[0:1]
	global_store_dword v[168:169], v175, off offset:1792
	ds_write_b128 v213, v[162:165] offset:7168
	s_cbranch_vccnz .LBB0_152
	s_add_i32 s12, s46, s14
	s_add_i32 s15, s12, 0xffffe000
	s_ashr_i32 s13, s12, 31
	s_cmpk_lt_i32 s12, 0x2000
	s_cselect_b32 s13, s13, 0
	s_cselect_b32 s12, s12, s15
	s_cselect_b32 s15, s37, s41
	s_cselect_b32 s16, s36, s40
	s_lshl_b64 s[12:13], s[12:13], 13
	s_add_u32 s12, s16, s12
	s_addc_u32 s13, s15, s13
	global_load_dwordx4 v[158:161], v182, s[12:13] nt
	global_load_dwordx4 v[154:157], v182, s[12:13] offset:1024 nt
	global_load_dwordx4 v[150:153], v182, s[12:13] offset:2048 nt
	global_load_dwordx4 v[146:149], v182, s[12:13] offset:3072 nt
	global_load_dwordx4 v[142:145], v170, s[12:13] nt
	global_load_dwordx4 v[138:141], v171, s[12:13] nt
	global_load_dwordx4 v[134:137], v172, s[12:13] nt
	global_load_dwordx4 v[130:133], v173, s[12:13] nt
